# baseline (speedup 1.0000x reference)
.Lproj_go_15:
	s_waitcnt vmcnt(8)
	v_mfma_f32_16x16x32_f16 v[100:103], v[10:13], v[116:119], v[100:103]
	ds_read_b128 v[128:131], v59
	ds_read_b128 v[132:135], v132
	v_or_b32_e32 v59, 0x1f000, v57
	v_or_b32_e32 v57, 0x1f800, v57
	s_waitcnt vmcnt(7)
	v_mfma_f32_16x16x32_f16 v[104:107], v[6:9], v[116:119], v[104:107]
	ds_read_b128 v[136:139], v59
	ds_read_b128 v[140:143], v57
	v_or_b32_e32 v57, 0x1e000, v58
	v_or_b32_e32 v59, 0x1e800, v58
	s_waitcnt vmcnt(6)
	v_mfma_f32_16x16x32_f16 v[68:71], v[116:119], v[2:5], v[68:71]
	ds_read_b128 v[116:119], v57
	ds_read_b128 v[144:147], v59
	v_or_b32_e32 v57, 0x1f000, v58
	v_or_b32_e32 v58, 0x1f800, v58
	s_waitcnt vmcnt(5) lgkmcnt(5)
	v_mfma_f32_16x16x32_f16 v[100:103], v[38:41], v[128:131], v[100:103]
	ds_read_b128 v[148:151], v57
	ds_read_b128 v[152:155], v58
	v_lshl_add_u64 v[58:59], s[4:5], 0, v[54:55]
	v_and_b32_e32 v54, 48, v0
	s_waitcnt vmcnt(4)
	v_mfma_f32_16x16x32_f16 v[104:107], v[34:37], v[128:131], v[104:107]
	s_lshl_b32 s4, s16, 5
	s_waitcnt vmcnt(3)
	v_mfma_f32_16x16x32_f16 v[68:71], v[128:131], v[30:33], v[68:71]
	v_lshl_add_u64 v[128:129], v[58:59], 0, v[54:55]
	s_waitcnt vmcnt(2) lgkmcnt(3)
	v_mfma_f32_16x16x32_f16 v[100:103], v[22:25], v[116:119], v[100:103]
	s_waitcnt vmcnt(1)
	v_mfma_f32_16x16x32_f16 v[104:107], v[26:29], v[116:119], v[104:107]
	s_waitcnt vmcnt(0)
	v_mfma_f32_16x16x32_f16 v[68:71], v[116:119], v[18:21], v[68:71]
	s_nop 3
	v_mov_b32_e32 v54, v101
	v_mov_b32_e32 v55, v102
	v_pk_mul_f32 v[54:55], v[54:55], s[2:3] op_sel_hi:[1,0]
	v_mfma_f32_16x16x32_f16 v[76:79], v[10:13], v[120:123], v[76:79]
	v_fma_mixlo_f16 v57, v100, s2, 0
	v_cvt_pk_f16_f32 v100, v54, v55
	v_mov_b32_e32 v54, v105
	v_mov_b32_e32 v55, v106
	v_mfma_f32_16x16x32_f16 v[84:87], v[6:9], v[120:123], v[84:87]
	v_mul_f32_e64 v54, v54, s2
	v_mul_f32_e64 v55, v55, s2
	v_pack_b32_f16 v58, v57, v100
	v_cvt_pk_f16_f32 v57, v54, v55
	v_mov_b32_e32 v54, v69
	v_mfma_f32_16x16x32_f16 v[88:91], v[120:123], v[2:5], v[88:91]
	v_mov_b32_e32 v55, v70
	v_pk_mul_f32 v[54:55], v[54:55], s[2:3] op_sel_hi:[1,0]
	v_fma_mixlo_f16 v59, v104, s2, 0
	v_mfma_f32_16x16x32_f16 v[76:79], v[38:41], v[132:135], v[76:79]
	v_cvt_pk_f16_f32 v70, v54, v55
	v_fma_mixlo_f16 v54, v103, s2, 0
	v_fma_mixlo_f16 v104, v68, s2, 0
	v_mfma_f32_16x16x32_f16 v[84:87], v[34:37], v[132:135], v[84:87]
	v_pack_b32_f16 v68, v59, v57
	v_alignbit_b32 v59, v54, v100, 16
	v_fma_mixlo_f16 v54, v107, s2, 0
	v_alignbit_b32 v69, v54, v57, 16
	v_lshlrev_b64 v[100:101], 7, v[156:157]
	v_mfma_f32_16x16x32_f16 v[88:91], v[132:135], v[30:33], v[88:91]
	v_lshl_or_b32 v105, v56, 3, s4
	v_or_b32_e32 v100, v100, v105
	v_lshl_add_u64 v[102:103], s[6:7], 0, v[100:101]
	s_waitcnt lgkmcnt(2)
	v_mfma_f32_16x16x32_f16 v[54:57], v[22:25], v[144:147], v[76:79]
	v_subrev_u32_e32 v170, s21, v102
	ds_write_b64 v170, v[58:59]
	v_lshl_add_u64 v[58:59], s[8:9], 0, v[100:101]
	v_subrev_u32_e32 v170, s22, v58
	ds_write_b64 v170, v[68:69]
	v_mfma_f32_16x16x32_f16 v[76:79], v[26:29], v[144:147], v[84:87]
	v_or_b32_e32 v68, 16, v156
	s_nop 2
	v_fma_mixlo_f16 v58, v54, s2, 0
	v_mov_b32_e32 v54, v55
	v_mfma_f32_16x16x32_f16 v[84:87], v[144:147], v[18:21], v[88:91]
	v_mov_b32_e32 v55, v56
	v_pk_mul_f32 v[54:55], v[54:55], s[2:3] op_sel_hi:[1,0]
	v_fma_mixlo_f16 v59, v76, s2, 0
	v_mfma_f32_16x16x32_f16 v[60:63], v[46:49], v[80:83], v[60:63]
	v_cvt_pk_f16_f32 v56, v54, v55
	v_mov_b32_e32 v54, v77
	v_mov_b32_e32 v55, v78
	v_mfma_f32_16x16x32_f16 v[72:75], v[42:45], v[80:83], v[72:75]
	v_mul_f32_e64 v54, v54, s2
	v_mul_f32_e64 v55, v55, s2
	v_pack_b32_f16 v76, v58, v56
	v_ashrrev_i32_e32 v69, 31, v68
	v_mfma_f32_16x16x32_f16 v[80:83], v[80:83], v[14:17], v[92:95]
	v_lshlrev_b64 v[68:69], 7, v[68:69]
	v_or_b32_e32 v68, v68, v105
	v_fma_mixlo_f16 v84, v84, s2, 0
	v_mfma_f32_16x16x32_f16 v[42:45], v[42:45], v[112:115], v[64:67]
	s_nop 2
	v_cvt_pk_f16_f32 v67, v54, v55
	v_mov_b32_e32 v54, v85
	v_mov_b32_e32 v55, v86
	v_pk_mul_f32 v[54:55], v[54:55], s[2:3] op_sel_hi:[1,0]
	v_pack_b32_f16 v66, v59, v67
	v_mfma_f32_16x16x32_f16 v[58:61], v[10:13], v[96:99], v[60:63]
	v_mfma_f32_16x16x32_f16 v[62:65], v[6:9], v[96:99], v[72:75]
	s_nop 2
	v_cvt_pk_f16_f32 v74, v54, v55
	v_fma_mixlo_f16 v54, v57, s2, 0
	v_alignbit_b32 v77, v54, v56, 16
	v_mfma_f32_16x16x32_f16 v[54:57], v[96:99], v[2:5], v[80:83]
	v_fma_mixlo_f16 v72, v79, s2, 0
	v_alignbit_b32 v67, v72, v67, 16
	v_lshl_add_u64 v[72:73], s[6:7], 0, v[68:69]
	v_mfma_f32_16x16x32_f16 v[46:49], v[46:49], v[112:115], v[108:111]
	v_lshl_add_u64 v[68:69], s[8:9], 0, v[68:69]
	v_subrev_u32_e32 v170, s22, v68
	ds_write_b64 v170, v[66:67]
	v_lshrrev_b32_e32 v67, 16, v70
	v_mfma_f32_16x16x32_f16 v[58:61], v[38:41], v[136:139], v[58:61]
	v_lshrrev_b32_e32 v69, 16, v74
	v_fma_mixhi_f16 v69, v87, s2, 0
	v_fma_mixhi_f16 v67, v71, s2, 0
	v_mfma_f32_16x16x32_f16 v[54:57], v[136:139], v[30:33], v[54:57]
	v_pack_b32_f16 v68, v84, v74
	v_pack_b32_f16 v66, v104, v70
	v_subrev_u32_e32 v170, s23, v128
	ds_write_b128 v170, v[66:69]
	v_mfma_f32_16x16x32_f16 v[62:65], v[34:37], v[136:139], v[62:65]
	v_subrev_u32_e32 v170, s21, v72
	ds_write_b64 v170, v[76:77]
	v_or_b32_e32 v66, 32, v156
	v_ashrrev_i32_e32 v67, 31, v66
	v_mfma_f32_16x16x32_f16 v[14:17], v[112:115], v[14:17], v[50:53]
	v_mfma_f32_16x16x32_f16 v[6:9], v[6:9], v[124:127], v[42:45]
	s_waitcnt lgkmcnt(1)
	v_mfma_f32_16x16x32_f16 v[58:61], v[22:25], v[148:151], v[58:61]
	v_mfma_f32_16x16x32_f16 v[54:57], v[148:151], v[18:21], v[54:57]
	v_mfma_f32_16x16x32_f16 v[10:13], v[10:13], v[124:127], v[46:49]
	s_nop 5
	v_fma_mixlo_f16 v68, v58, s2, 0
	v_mov_b32_e32 v58, v59
	v_mov_b32_e32 v59, v60
	v_mfma_f32_16x16x32_f16 v[62:65], v[26:29], v[148:151], v[62:65]
	v_mul_f32_e64 v50, v58, s2
	v_mul_f32_e64 v51, v59, s2
	v_fma_mixlo_f16 v54, v54, s2, 0
	v_cvt_pk_f16_f32 v50, v50, v51
	v_mfma_f32_16x16x32_f16 v[2:5], v[124:127], v[2:5], v[14:17]
	v_pack_b32_f16 v46, v68, v50
	s_nop 1
	v_mov_b32_e32 v48, v63
	v_mov_b32_e32 v49, v64
	v_mfma_f32_16x16x32_f16 v[6:9], v[34:37], v[140:143], v[6:9]
	v_mov_b32_e32 v14, v55
	v_mov_b32_e32 v15, v56
	v_pk_mul_f32 v[14:15], v[14:15], s[2:3] op_sel_hi:[1,0]
	v_mfma_f32_16x16x32_f16 v[10:13], v[38:41], v[140:143], v[10:13]
	v_mul_f32_e64 v42, v48, s2
	v_mul_f32_e64 v43, v49, s2
	v_cvt_pk_f16_f32 v38, v14, v15
	v_fma_mixlo_f16 v14, v61, s2, 0
	v_mfma_f32_16x16x32_f16 v[2:5], v[140:143], v[30:33], v[2:5]
	v_fma_mixlo_f16 v62, v62, s2, 0
	v_cvt_pk_f16_f32 v43, v42, v43
	v_alignbit_b32 v47, v14, v50, 16
	v_fma_mixlo_f16 v14, v65, s2, 0
	s_waitcnt lgkmcnt(0)
	v_mfma_f32_16x16x32_f16 v[6:9], v[26:29], v[152:155], v[6:9]
	v_pack_b32_f16 v42, v62, v43
	v_alignbit_b32 v43, v14, v43, 16
	v_lshlrev_b64 v[14:15], 7, v[66:67]
	v_mfma_f32_16x16x32_f16 v[10:13], v[22:25], v[152:155], v[10:13]
	v_or_b32_e32 v14, v14, v105
	v_lshl_add_u64 v[16:17], s[6:7], 0, v[14:15]
	v_subrev_u32_e32 v170, s21, v16
	ds_write_b64 v170, v[46:47]
	v_mfma_f32_16x16x32_f16 v[2:5], v[152:155], v[18:21], v[2:5]
	v_lshl_add_u64 v[14:15], s[8:9], 0, v[14:15]
	v_fma_mixlo_f16 v17, v6, s2, 0
	v_mov_b32_e32 v6, v7
	v_mov_b32_e32 v7, v8
	v_subrev_u32_e32 v170, s22, v14
	ds_write_b64 v170, v[42:43]
	v_or_b32_e32 v14, 48, v156
	v_fma_mixlo_f16 v16, v10, s2, 0
	v_mov_b32_e32 v10, v11
	v_mov_b32_e32 v11, v12
	v_pk_mul_f32 v[6:7], v[6:7], s[2:3] op_sel_hi:[1,0]
	v_ashrrev_i32_e32 v15, 31, v14
	v_pk_mul_f32 v[10:11], v[10:11], s[2:3] op_sel_hi:[1,0]
	v_cvt_pk_f16_f32 v7, v6, v7
	v_fma_mixlo_f16 v8, v9, s2, 0
	v_cvt_pk_f16_f32 v12, v10, v11
	v_pack_b32_f16 v6, v17, v7
	v_mov_b32_e32 v10, v3
	v_mov_b32_e32 v11, v4
	v_alignbit_b32 v7, v8, v7, 16
	v_lshlrev_b64 v[8:9], 7, v[14:15]
	v_pk_mul_f32 v[10:11], v[10:11], s[2:3] op_sel_hi:[1,0]
	v_fma_mixlo_f16 v3, v13, s2, 0
	v_or_b32_e32 v8, v8, v105
	v_fma_mixlo_f16 v18, v2, s2, 0
	v_pack_b32_f16 v2, v16, v12
	v_cvt_pk_f16_f32 v4, v10, v11
	v_alignbit_b32 v3, v3, v12, 16
	v_lshl_add_u64 v[10:11], s[6:7], 0, v[8:9]
	v_subrev_u32_e32 v170, s21, v10
	ds_write_b64 v170, v[2:3]
	v_lshl_add_u64 v[2:3], s[8:9], 0, v[8:9]
	v_subrev_u32_e32 v170, s22, v2
	ds_write_b64 v170, v[6:7]
	v_lshrrev_b32_e32 v7, 16, v38
	v_lshrrev_b32_e32 v9, 16, v4
	v_fma_mixhi_f16 v9, v5, s2, 0
	v_fma_mixhi_f16 v7, v57, s2, 0
	v_pack_b32_f16 v8, v18, v4
	v_pack_b32_f16 v6, v54, v38
	v_subrev_u32_e32 v170, s23, v128
	ds_write_b128 v170, v[6:9] offset:64
	s_waitcnt lgkmcnt(0)
	s_barrier
	v_and_b32_e32 v170, 63, v0
	v_lshlrev_b32_e32 v170, 4, v170
	v_lshl_add_u32 v170, s16, 10, v170
	v_add_u32_e32 v168, s24, v170
	v_add_u32_e32 v169, 0x1000, v168
	v_add_u32_e32 v170, 0x20100, v170
	ds_read_b128 v[160:163], v170
	ds_read_b128 v[164:167], v170 offset:4096
	ds_read_b128 v[172:175], v170 offset:8192
	s_waitcnt lgkmcnt(2)
	global_store_dwordx4 v168, v[160:163], s[6:7] sc0 sc1
	s_waitcnt lgkmcnt(1)
	global_store_dwordx4 v169, v[164:167], s[6:7] sc0 sc1
	s_waitcnt lgkmcnt(0)
	global_store_dwordx4 v168, v[172:175], s[8:9] sc0 sc1
	s_nop 1
	ds_read_b128 v[160:163], v170 offset:12288
	ds_read_b128 v[164:167], v170 offset:16384
	ds_read_b128 v[172:175], v170 offset:20480
	s_waitcnt lgkmcnt(2)
	global_store_dwordx4 v169, v[160:163], s[8:9] sc0 sc1
	s_waitcnt lgkmcnt(1)
	global_store_dwordx4 v168, v[164:167], s[10:11] sc0 sc1
	s_waitcnt lgkmcnt(0)
	global_store_dwordx4 v169, v[172:175], s[10:11] sc0 sc1
	s_endpgm

.LBB2_24:
	s_cmp_lg_u32 s40, 0
	s_cselect_b64 s[4:5], -1, 0
	s_cmp_lg_u32 s62, s61
	s_cselect_b64 s[6:7], -1, 0
	s_or_b64 s[6:7], s[4:5], s[6:7]
	s_mov_b64 s[4:5], -1
	s_and_b64 vcc, exec, s[6:7]
	s_cbranch_vccz .LBB2_28
	v_div_scale_f32 v15, s[4:5], v14, v14, 1.0
	v_rcp_f32_e32 v17, v15
	v_mov_b32_e32 v33, v28
	v_mov_b32_e32 v67, v51
	v_fma_f32 v30, -v15, v17, 1.0
	v_fmac_f32_e32 v17, v30, v17
	v_div_scale_f32 v30, vcc, 1.0, v14, 1.0
	v_mul_f32_e32 v31, v30, v17
	v_fma_f32 v32, -v15, v31, v30
	v_fmac_f32_e32 v31, v32, v17
	v_fma_f32 v15, -v15, v31, v30
	v_div_fmas_f32 v15, v15, v17, v31
	v_div_fixup_f32 v15, v15, v14, 1.0
	v_cmp_lt_f32_e32 vcc, 0, v14
	v_mov_b32_e32 v32, v27
	s_add_i32 s4, s76, s59
	v_cndmask_b32_e32 v30, 0, v15, vcc
	v_pk_mul_f32 v[32:33], v[30:31], v[32:33] op_sel_hi:[0,1]
	v_fma_mixlo_f16 v15, v30, v26, 0
	v_cvt_pk_f16_f32 v17, v32, v33
	v_pack_b32_f16 v32, v15, v17
	v_fma_mixlo_f16 v15, v30, v29, 0
	v_alignbit_b32 v33, v15, v17, 16
	ds_write_b64 v90, v[32:33] offset:32768
	v_mov_b32_e32 v32, v23
	v_mov_b32_e32 v33, v24
	v_pk_mul_f32 v[32:33], v[30:31], v[32:33] op_sel_hi:[0,1]
	v_fma_mixlo_f16 v15, v30, v22, 0
	v_cvt_pk_f16_f32 v17, v32, v33
	v_pack_b32_f16 v32, v15, v17
	v_fma_mixlo_f16 v15, v30, v25, 0
	v_alignbit_b32 v33, v15, v17, 16
	ds_write_b64 v91, v[32:33] offset:32768
	v_mov_b32_e32 v32, v19
	v_mov_b32_e32 v33, v20
	v_pk_mul_f32 v[32:33], v[30:31], v[32:33] op_sel_hi:[0,1]
	v_fma_mixlo_f16 v15, v30, v18, 0
	v_cvt_pk_f16_f32 v17, v32, v33
	v_pack_b32_f16 v32, v15, v17
	v_fma_mixlo_f16 v15, v30, v21, 0
	v_alignbit_b32 v33, v15, v17, 16
	ds_write_b64 v92, v[32:33] offset:32768
	v_mov_b32_e32 v32, v11
	v_mov_b32_e32 v33, v12
	v_pk_mul_f32 v[32:33], v[30:31], v[32:33] op_sel_hi:[0,1]
	v_fma_mixlo_f16 v15, v30, v10, 0
	v_cvt_pk_f16_f32 v17, v32, v33
	v_pack_b32_f16 v32, v15, v17
	v_fma_mixlo_f16 v15, v30, v13, 0
	v_alignbit_b32 v33, v15, v17, 16
	s_ashr_i32 s5, s4, 31
	ds_write_b64 v93, v[32:33] offset:32768
	s_lshl_b64 s[4:5], s[4:5], 7
	s_add_u32 s4, s4, s52
	s_waitcnt vmcnt(0)
	ds_read_b128 v[30:33], v94 offset:32768
	ds_read_b128 v[34:37], v95 offset:32768
	s_addc_u32 s5, s5, 0
	s_lshl_b64 s[6:7], s[4:5], 7
	v_lshl_add_u64 v[38:39], v[60:61], 0, s[6:7]
	v_lshl_add_u64 v[40:41], v[38:39], 0, v[50:51]
	s_waitcnt lgkmcnt(1)
	global_store_dwordx4 v[40:41], v[30:33], off sc0 sc1
	s_nop 1
	v_lshl_add_u64 v[30:31], v[38:39], 0, v[66:67]
	s_waitcnt lgkmcnt(0)
	global_store_dwordx4 v[30:31], v[34:37], off sc0 sc1
	s_and_saveexec_b64 s[6:7], s[0:1]
	s_cbranch_execz .LBB2_27
	v_mov_b32_e32 v31, s5
	v_or_b32_e32 v30, s4, v56
	v_lshl_add_u64 v[30:31], v[30:31], 3, s[44:45]
	v_mov_b32_e32 v17, v14
	global_store_dwordx2 v[30:31], v[16:17], off sc0 sc1

.LBB2_28:
	s_andn2_b64 vcc, exec, s[4:5]
	s_cbranch_vccnz .LBB2_2
	v_div_scale_f32 v15, s[4:5], v14, v14, 1.0
	v_rcp_f32_e32 v16, v15
	v_div_scale_f32 v17, vcc, 1.0, v14, 1.0
	s_add_i32 s40, s54, s60
	v_fma_f32 v30, -v15, v16, 1.0
	v_fmac_f32_e32 v16, v30, v16
	v_mul_f32_e32 v30, v17, v16
	v_fma_f32 v31, -v15, v30, v17
	v_fmac_f32_e32 v30, v31, v16
	v_fma_f32 v15, -v15, v30, v17
	v_div_fmas_f32 v15, v15, v16, v30
	v_div_fixup_f32 v30, v15, v14, 1.0
	v_pk_mul_f32 v[16:17], v[30:31], v[28:29] op_sel_hi:[0,1]
	v_pk_mul_f32 v[14:15], v[30:31], v[26:27] op_sel_hi:[0,1]
	v_add_u32_e32 v26, v85, v86
	ds_write_b128 v26, v[14:17] offset:32768
	v_pk_mul_f32 v[16:17], v[30:31], v[24:25] op_sel_hi:[0,1]
	v_pk_mul_f32 v[14:15], v[30:31], v[22:23] op_sel_hi:[0,1]
	v_add_u32_e32 v22, v85, v87
	ds_write_b128 v22, v[14:17] offset:32768
	v_pk_mul_f32 v[16:17], v[30:31], v[20:21] op_sel_hi:[0,1]
	v_pk_mul_f32 v[14:15], v[30:31], v[18:19] op_sel_hi:[0,1]
	v_add_u32_e32 v18, v85, v88
	ds_write_b128 v18, v[14:17] offset:32768
	v_pk_mul_f32 v[12:13], v[30:31], v[12:13] op_sel_hi:[0,1]
	v_pk_mul_f32 v[10:11], v[30:31], v[10:11] op_sel_hi:[0,1]
	v_add_u32_e32 v14, v85, v89
	ds_write_b128 v14, v[10:13] offset:32768
	ds_read_b128 v[10:13], v96 offset:32768
	ds_read_b128 v[14:17], v97 offset:32768
	s_lshl_b64 s[4:5], s[40:41], 8
	v_lshl_add_u64 v[18:19], v[62:63], 0, s[4:5]
	v_mov_b32_e32 v69, v51
	v_lshl_add_u64 v[20:21], v[18:19], 0, v[68:69]
	v_mov_b32_e32 v71, v51
	s_waitcnt lgkmcnt(0)
	global_store_dwordx4 v[20:21], v[10:13], off sc0 sc1
	v_lshl_add_u64 v[20:21], v[18:19], 0, v[70:71]
	ds_read_b128 v[10:13], v98 offset:32768
	global_store_dwordx4 v[20:21], v[14:17], off sc0 sc1
	ds_read_b128 v[14:17], v99 offset:32768
	v_mov_b32_e32 v73, v51
	v_lshl_add_u64 v[20:21], v[18:19], 0, v[72:73]
	v_mov_b32_e32 v75, v51
	s_waitcnt lgkmcnt(0)
	global_store_dwordx4 v[20:21], v[10:13], off sc0 sc1
	s_nop 1
	v_lshl_add_u64 v[10:11], v[18:19], 0, v[74:75]
	global_store_dwordx4 v[10:11], v[14:17], off sc0 sc1
	s_branch .LBB2_2

_Z14combine_kernelPKDF16_PKfPf:
	s_load_dwordx4 s[4:7], s[0:1], 0x0
	s_load_dwordx2 s[10:11], s[0:1], 0x10
	s_lshl_b32 s3, s2, 5
	s_and_b32 s3, s3, 0x60
	s_lshr_b32 s8, s2, 5
	s_add_i32 s8, s8, s3
	s_lshl_b32 s9, s8, 5
	s_getpc_b64 s[12:13]
	s_add_u32 s12, s12, g_tab@rel32@lo+4
	s_addc_u32 s13, s13, g_tab@rel32@hi+12
	s_add_u32 s12, s12, s9
	s_addc_u32 s13, s13, 0
	s_load_dwordx8 s[16:23], s[12:13], 0x1a60
	s_lshl_b32 s2, s2, 2
	s_and_b32 s2, s2, 0x70
	v_lshrrev_b32_e32 v1, 4, v0
	v_or_b32_e32 v38, s2, v1
	v_lshlrev_b32_e32 v2, 2, v0
	v_and_b32_e32 v39, 60, v2
	v_lshlrev_b32_e32 v32, 3, v38
	v_lshlrev_b32_e32 v33, 7, v38
	v_lshl_add_u32 v33, v39, 1, v33
	v_lshlrev_b32_e32 v45, 8, v38
	v_lshl_add_u32 v45, v39, 2, v45
	s_add_i32 s0, s8, 3
	s_lshl_b32 s0, s0, 15
	s_mov_b32 s14, 0x7f800000
	s_mov_b32 s15, 0xf149f2ca
	s_waitcnt lgkmcnt(0)
	s_cmp_lt_i32 s17, 0
	s_cbranch_scc1 .Lcomb_end
	s_add_u32 s10, s10, s0
	s_addc_u32 s11, s11, 0
	s_lshl_b32 s24, s16, 10
	s_lshl_b32 s26, s16, 14
	s_add_u32 s24, s6, s24
	s_addc_u32 s25, s7, 0
	s_add_u32 s26, s4, s26
	s_addc_u32 s27, s5, 0
	global_load_dwordx2 v[0:1], v32, s[24:25] nt
	global_load_dwordx2 v[16:17], v33, s[26:27] nt
	s_lshl_b32 s28, s17, 10
	s_lshl_b32 s30, s17, 14
	s_add_u32 s28, s6, s28
	s_addc_u32 s29, s7, 0
	s_add_u32 s30, s4, s30
	s_addc_u32 s31, s5, 0
	global_load_dwordx2 v[2:3], v32, s[28:29] nt
	global_load_dwordx2 v[18:19], v33, s[30:31] nt
	s_cmp_lt_i32 s18, 0
	s_cselect_b32 s58, s15, s14
	s_cselect_b32 s1, s16, s18
	s_lshl_b32 s32, s1, 10
	s_lshl_b32 s34, s1, 14
	s_add_u32 s32, s6, s32
	s_addc_u32 s33, s7, 0
	s_add_u32 s34, s4, s34
	s_addc_u32 s35, s5, 0
	global_load_dwordx2 v[4:5], v32, s[32:33] nt
	global_load_dwordx2 v[20:21], v33, s[34:35] nt
	s_cmp_lt_i32 s19, 0
	s_cselect_b32 s59, s15, s14
	s_cselect_b32 s1, s16, s19
	s_lshl_b32 s36, s1, 10
	s_lshl_b32 s38, s1, 14
	s_add_u32 s36, s6, s36
	s_addc_u32 s37, s7, 0
	s_add_u32 s38, s4, s38
	s_addc_u32 s39, s5, 0
	global_load_dwordx2 v[6:7], v32, s[36:37] nt
	global_load_dwordx2 v[22:23], v33, s[38:39] nt
	s_cmp_lt_i32 s20, 0
	s_cselect_b32 s60, s15, s14
	s_cselect_b32 s1, s16, s20
	s_lshl_b32 s40, s1, 10
	s_lshl_b32 s42, s1, 14
	s_add_u32 s40, s6, s40
	s_addc_u32 s41, s7, 0
	s_add_u32 s42, s4, s42
	s_addc_u32 s43, s5, 0
	global_load_dwordx2 v[8:9], v32, s[40:41] nt
	global_load_dwordx2 v[24:25], v33, s[42:43] nt
	s_cmp_lt_i32 s21, 0
	s_cselect_b32 s61, s15, s14
	s_cselect_b32 s1, s16, s21
	s_lshl_b32 s44, s1, 10
	s_lshl_b32 s46, s1, 14
	s_add_u32 s44, s6, s44
	s_addc_u32 s45, s7, 0
	s_add_u32 s46, s4, s46
	s_addc_u32 s47, s5, 0
	global_load_dwordx2 v[10:11], v32, s[44:45] nt
	global_load_dwordx2 v[26:27], v33, s[46:47] nt
	s_cmp_lt_i32 s22, 0
	s_cselect_b32 s62, s15, s14
	s_cselect_b32 s1, s16, s22
	s_lshl_b32 s48, s1, 10
	s_lshl_b32 s50, s1, 14
	s_add_u32 s48, s6, s48
	s_addc_u32 s49, s7, 0
	s_add_u32 s50, s4, s50
	s_addc_u32 s51, s5, 0
	global_load_dwordx2 v[12:13], v32, s[48:49] nt
	global_load_dwordx2 v[28:29], v33, s[50:51] nt
	s_cmp_lt_i32 s23, 0
	s_cselect_b32 s63, s15, s14
	s_cselect_b32 s1, s16, s23
	s_lshl_b32 s52, s1, 10
	s_lshl_b32 s54, s1, 14
	s_add_u32 s52, s6, s52
	s_addc_u32 s53, s7, 0
	s_add_u32 s54, s4, s54
	s_addc_u32 s55, s5, 0
	global_load_dwordx2 v[14:15], v32, s[52:53] nt
	global_load_dwordx2 v[30:31], v33, s[54:55] nt
	s_waitcnt vmcnt(0)
	v_min_f32_e32 v4, s58, v4
	v_min_f32_e32 v6, s59, v6
	v_min_f32_e32 v8, s60, v8
	v_min_f32_e32 v10, s61, v10
	v_min_f32_e32 v12, s62, v12
	v_min_f32_e32 v14, s63, v14
	v_max3_f32 v34, v0, v2, v4
	v_max3_f32 v34, v34, v6, v8
	v_max3_f32 v34, v34, v10, v12
	v_max_f32_e32 v34, v34, v14
	v_sub_f32_e32 v0, v0, v34
	v_sub_f32_e32 v2, v2, v34
	v_sub_f32_e32 v4, v4, v34
	v_sub_f32_e32 v6, v6, v34
	v_sub_f32_e32 v8, v8, v34
	v_sub_f32_e32 v10, v10, v34
	v_sub_f32_e32 v12, v12, v34
	v_sub_f32_e32 v14, v14, v34
	v_exp_f32_e32 v0, v0
	v_exp_f32_e32 v2, v2
	v_exp_f32_e32 v4, v4
	v_exp_f32_e32 v6, v6
	v_exp_f32_e32 v8, v8
	v_exp_f32_e32 v10, v10
	v_exp_f32_e32 v12, v12
	v_exp_f32_e32 v14, v14
	s_nop 0
	v_mul_f32_e32 v0, v0, v1
	v_mul_f32_e32 v2, v2, v3
	v_mul_f32_e32 v4, v4, v5
	v_mul_f32_e32 v6, v6, v7
	v_mul_f32_e32 v8, v8, v9
	v_mul_f32_e32 v10, v10, v11
	v_mul_f32_e32 v12, v12, v13
	v_mul_f32_e32 v14, v14, v15
	v_cvt_f32_f16_e32 v40, v16
	v_cvt_f32_f16_sdwa v41, v16 dst_sel:DWORD dst_unused:UNUSED_PAD src0_sel:WORD_1
	v_cvt_f32_f16_e32 v42, v17
	v_cvt_f32_f16_sdwa v43, v17 dst_sel:DWORD dst_unused:UNUSED_PAD src0_sel:WORD_1
	v_mul_f32_e32 v34, v40, v0
	v_mul_f32_e32 v35, v41, v0
	v_mul_f32_e32 v36, v42, v0
	v_mul_f32_e32 v37, v43, v0
	v_mov_b32_e32 v44, v0
	v_cvt_f32_f16_e32 v40, v18
	v_cvt_f32_f16_sdwa v41, v18 dst_sel:DWORD dst_unused:UNUSED_PAD src0_sel:WORD_1
	v_cvt_f32_f16_e32 v42, v19
	v_cvt_f32_f16_sdwa v43, v19 dst_sel:DWORD dst_unused:UNUSED_PAD src0_sel:WORD_1
	v_fmac_f32_e32 v34, v40, v2
	v_fmac_f32_e32 v35, v41, v2
	v_fmac_f32_e32 v36, v42, v2
	v_fmac_f32_e32 v37, v43, v2
	v_add_f32_e32 v44, v44, v2
	v_cvt_f32_f16_e32 v40, v20
	v_cvt_f32_f16_sdwa v41, v20 dst_sel:DWORD dst_unused:UNUSED_PAD src0_sel:WORD_1
	v_cvt_f32_f16_e32 v42, v21
	v_cvt_f32_f16_sdwa v43, v21 dst_sel:DWORD dst_unused:UNUSED_PAD src0_sel:WORD_1
	v_fmac_f32_e32 v34, v40, v4
	v_fmac_f32_e32 v35, v41, v4
	v_fmac_f32_e32 v36, v42, v4
	v_fmac_f32_e32 v37, v43, v4
	v_add_f32_e32 v44, v44, v4
	v_cvt_f32_f16_e32 v40, v22
	v_cvt_f32_f16_sdwa v41, v22 dst_sel:DWORD dst_unused:UNUSED_PAD src0_sel:WORD_1
	v_cvt_f32_f16_e32 v42, v23
	v_cvt_f32_f16_sdwa v43, v23 dst_sel:DWORD dst_unused:UNUSED_PAD src0_sel:WORD_1
	v_fmac_f32_e32 v34, v40, v6
	v_fmac_f32_e32 v35, v41, v6
	v_fmac_f32_e32 v36, v42, v6
	v_fmac_f32_e32 v37, v43, v6
	v_add_f32_e32 v44, v44, v6
	v_cvt_f32_f16_e32 v40, v24
	v_cvt_f32_f16_sdwa v41, v24 dst_sel:DWORD dst_unused:UNUSED_PAD src0_sel:WORD_1
	v_cvt_f32_f16_e32 v42, v25
	v_cvt_f32_f16_sdwa v43, v25 dst_sel:DWORD dst_unused:UNUSED_PAD src0_sel:WORD_1
	v_fmac_f32_e32 v34, v40, v8
	v_fmac_f32_e32 v35, v41, v8
	v_fmac_f32_e32 v36, v42, v8
	v_fmac_f32_e32 v37, v43, v8
	v_add_f32_e32 v44, v44, v8
	v_cvt_f32_f16_e32 v40, v26
	v_cvt_f32_f16_sdwa v41, v26 dst_sel:DWORD dst_unused:UNUSED_PAD src0_sel:WORD_1
	v_cvt_f32_f16_e32 v42, v27
	v_cvt_f32_f16_sdwa v43, v27 dst_sel:DWORD dst_unused:UNUSED_PAD src0_sel:WORD_1
	v_fmac_f32_e32 v34, v40, v10
	v_fmac_f32_e32 v35, v41, v10
	v_fmac_f32_e32 v36, v42, v10
	v_fmac_f32_e32 v37, v43, v10
	v_add_f32_e32 v44, v44, v10
	v_cvt_f32_f16_e32 v40, v28
	v_cvt_f32_f16_sdwa v41, v28 dst_sel:DWORD dst_unused:UNUSED_PAD src0_sel:WORD_1
	v_cvt_f32_f16_e32 v42, v29
	v_cvt_f32_f16_sdwa v43, v29 dst_sel:DWORD dst_unused:UNUSED_PAD src0_sel:WORD_1
	v_fmac_f32_e32 v34, v40, v12
	v_fmac_f32_e32 v35, v41, v12
	v_fmac_f32_e32 v36, v42, v12
	v_fmac_f32_e32 v37, v43, v12
	v_add_f32_e32 v44, v44, v12
	v_cvt_f32_f16_e32 v40, v30
	v_cvt_f32_f16_sdwa v41, v30 dst_sel:DWORD dst_unused:UNUSED_PAD src0_sel:WORD_1
	v_cvt_f32_f16_e32 v42, v31
	v_cvt_f32_f16_sdwa v43, v31 dst_sel:DWORD dst_unused:UNUSED_PAD src0_sel:WORD_1
	v_fmac_f32_e32 v34, v40, v14
	v_fmac_f32_e32 v35, v41, v14
	v_fmac_f32_e32 v36, v42, v14
	v_fmac_f32_e32 v37, v43, v14
	v_add_f32_e32 v44, v44, v14
	v_div_scale_f32 v14, s[0:1], v44, v44, 1.0
	v_div_scale_f32 v2, vcc, 1.0, v44, 1.0
	v_rcp_f32_e32 v15, v14
	s_nop 0
	v_fma_f32 v3, -v14, v15, 1.0
	v_fmac_f32_e32 v15, v3, v15
	v_mul_f32_e32 v3, v2, v15
	v_fma_f32 v6, -v14, v3, v2
	v_fmac_f32_e32 v3, v6, v15
	v_fma_f32 v2, -v14, v3, v2
	v_div_fmas_f32 v2, v2, v15, v3
	v_div_fixup_f32 v6, v2, v44, 1.0
	v_mul_f32_e32 v34, v34, v6
	v_mul_f32_e32 v35, v35, v6
	v_mul_f32_e32 v36, v36, v6
	v_mul_f32_e32 v37, v37, v6
	global_store_dwordx4 v45, v[34:37], s[10:11] sc0 sc1
